# v8 plus an early L2 write-back by the first workgroup of each XCD to arrive at a barrier
# baseline (speedup 1.0000x reference)
.LBB0_781:
	v_readlane_b32 s6, v254, 17
	v_readlane_b32 s7, v254, 18
	v_cvt_f32_u32_e32 v1, v2
	v_sub_u32_e32 v4, 0, v2
	v_rcp_iflag_f32_e32 v1, v1
	s_nop 1
	buffer_inv sc1
	global_atomic_add v3, v65, v167, s[6:7] sc0
	v_mul_f32_e32 v1, 0x4f7ffffe, v1
	v_cvt_u32_f32_e32 v1, v1
	v_mul_lo_u32 v4, v4, v1
	v_mul_hi_u32 v4, v1, v4
	v_add_u32_e32 v1, v1, v4
	s_waitcnt vmcnt(0)
	v_mul_hi_u32 v1, v3, v1
	v_mul_lo_u32 v4, v1, v2
	v_sub_u32_e32 v4, v3, v4
	v_add_u32_e32 v5, 1, v1
	v_cmp_ge_u32_e32 vcc, v4, v2
	v_add_u32_e32 v3, 1, v3
	s_nop 0
	v_cndmask_b32_e32 v1, v1, v5, vcc
	v_sub_u32_e32 v5, v4, v2
	v_cndmask_b32_e32 v4, v4, v5, vcc
	v_add_u32_e32 v5, 1, v1
	v_cmp_ge_u32_e32 vcc, v4, v2
	s_nop 1
	v_cndmask_b32_e32 v1, v1, v5, vcc
	v_mul_lo_u32 v4, v2, v1
	v_add_u32_e32 v2, v4, v2
	v_cmp_ne_u32_e32 vcc, v3, v2
	s_and_saveexec_b64 s[6:7], vcc
	s_xor_b64 s[6:7], exec, s[6:7]
	s_cbranch_execz .LBB0_795
	v_add_u32_e32 v5, 1, v4
	v_cmp_eq_u32_e32 vcc, v3, v5
	s_and_saveexec_b64 s[8:9], vcc
	buffer_wbl2 sc1
	s_or_b64 exec, exec, s[8:9]
	v_readlane_b32 s8, v254, 19
	v_readlane_b32 s9, v254, 20
	s_waitcnt lgkmcnt(0)
	s_nop 3
	global_load_dword v0, v65, s[8:9] sc1
	s_waitcnt vmcnt(0)
	v_cmp_eq_u32_e32 vcc, v0, v1
	s_and_saveexec_b64 s[8:9], vcc
	s_cbranch_execz .LBB0_794
	s_mov_b32 s21, 1
	s_mov_b64 s[10:11], 0
	s_branch .LBB0_785

.LBB0_2518:
	v_readlane_b32 s6, v254, 17
	v_readlane_b32 s7, v254, 18
	v_cvt_f32_u32_e32 v1, v2
	v_sub_u32_e32 v4, 0, v2
	v_rcp_iflag_f32_e32 v1, v1
	s_nop 1
	buffer_inv sc1
	global_atomic_add v3, v65, v167, s[6:7] sc0
	v_mul_f32_e32 v1, 0x4f7ffffe, v1
	v_cvt_u32_f32_e32 v1, v1
	v_mul_lo_u32 v4, v4, v1
	v_mul_hi_u32 v4, v1, v4
	v_add_u32_e32 v1, v1, v4
	s_waitcnt vmcnt(0)
	v_mul_hi_u32 v1, v3, v1
	v_mul_lo_u32 v4, v1, v2
	v_sub_u32_e32 v4, v3, v4
	v_add_u32_e32 v5, 1, v1
	v_cmp_ge_u32_e32 vcc, v4, v2
	v_add_u32_e32 v3, 1, v3
	s_nop 0
	v_cndmask_b32_e32 v1, v1, v5, vcc
	v_sub_u32_e32 v5, v4, v2
	v_cndmask_b32_e32 v4, v4, v5, vcc
	v_add_u32_e32 v5, 1, v1
	v_cmp_ge_u32_e32 vcc, v4, v2
	s_nop 1
	v_cndmask_b32_e32 v1, v1, v5, vcc
	v_mul_lo_u32 v4, v2, v1
	v_add_u32_e32 v2, v4, v2
	v_cmp_ne_u32_e32 vcc, v3, v2
	s_and_saveexec_b64 s[6:7], vcc
	s_xor_b64 s[6:7], exec, s[6:7]
	s_cbranch_execz .LBB0_2532
	v_add_u32_e32 v5, 1, v4
	v_cmp_eq_u32_e32 vcc, v3, v5
	s_and_saveexec_b64 s[8:9], vcc
	buffer_wbl2 sc1
	s_or_b64 exec, exec, s[8:9]
	v_readlane_b32 s8, v254, 19
	v_readlane_b32 s9, v254, 20
	s_waitcnt lgkmcnt(0)
	s_nop 3
	global_load_dword v0, v65, s[8:9] sc1
	s_waitcnt vmcnt(0)
	v_cmp_eq_u32_e32 vcc, v0, v1
	s_and_saveexec_b64 s[8:9], vcc
	s_cbranch_execz .LBB0_2531
	s_mov_b32 s20, 1
	s_mov_b64 s[10:11], 0
	s_branch .LBB0_2522
